# gating phase: all V/U/W/gain loads of a unit issued up front with counted vmcnt (was 24 serialized load round trips per unit)
# speedup vs baseline: 1.0057x; 1.0057x over previous
; #define GAS __attribute__((address_space(1)))
; #define LAS __attribute__((address_space(3)))
; __device__ __forceinline__ u32x4 pack8f(const f32x4 a, const f32x4 b) { u32x4 w; w.x = pk2(a[0], a[1]); w.y = pk2(a[2], a[3]); w.z = pk2(b[0], b[1]); w.w = pk2(b[2], b[3]); return w; }
; __device__ __forceinline__ void gating_phase(Frame& F) {
;     ...
;     for (int unit = F.vcu; unit < 2048; unit += F.G) {
;         const int chunk = unit >> 3, g = unit & 7, row0 = chunk * GMC;
;         if (F.tid < GMC) { const GAS f32x4* sp = (const GAS f32x4*)(lnsp + (size_t)(row0 + F.tid) * 64); float s1 = 0.f, s2 = 0.f;
; #pragma unroll
;             for (int j = 0; j < 16; ++j) { const f32x4 v = sp[j]; s1 += v[0] + v[2]; s2 += v[1] + v[3]; }
;             const float mean = s1 * (1.f / GMW); float var = s2 * (1.f / GMW) - mean * mean; var = var > 0.f ? var : 0.f;
;             lst[F.tid] = (f32x2){mean, __builtin_amdgcn_rsqf(var + EPSN)}; }
;         __syncthreads();
; #pragma unroll 2
;         for (int i = 0; i < 8; ++i) { const int idx = F.tid + 512 * i, r = idx >> 5, ch = idx & 31;
;             const u32x4 raw = *(const GAS u32x4*)(V + (size_t)(row0 + r) * GMW + g * GMGD + ch * 8);
;             const f32x2 st = lst[r]; const float mean = st.x, rstd = st.y;
;             const f32x4 g0 = *(const f32x4*)(lng + g * GMGD + ch * 8), g1 = *(const f32x4*)(lng + g * GMGD + ch * 8 + 4), b0 = *(const f32x4*)(lnb + g * GMGD + ch * 8), b1 = *(const f32x4*)(lnb + g * GMGD + ch * 8 + 4);
;             f32x4 x0 = {bf_lo(raw.x), bf_hi(raw.x), bf_lo(raw.y), bf_hi(raw.y)}, x1 = {bf_lo(raw.z), bf_hi(raw.z), bf_lo(raw.w), bf_hi(raw.w)};
;             x0 = (x0 - mean) * rstd * g0 + b0; x1 = (x1 - mean) * rstd * g1 + b1;
;             *(LAS u32x4*)(vl + r * VSTG + ch * 16) = pack8f(x0, x1); }
;         __syncthreads();
;         const bf16* wrow = WSB + ((size_t)g * GMC + 16 * F.wave + c) * GMC + 4 * kq;
;         bf16x8 wf[4];
; #pragma unroll
;         for (int sl = 0; sl < 4; ++sl) { const u32x2 lo = *(const GAS u32x2*)(wrow + 32 * sl), hi = *(const GAS u32x2*)(wrow + 32 * sl + 16); u32x4 w = {lo.x, lo.y, hi.x, hi.y}; wf[sl] = __builtin_bit_cast(bf16x8, w); }
;         const int t = row0 + 16 * F.wave + c; const float bst = bsp[g * GMC + 16 * F.wave + c];
;         bf16* urow = U + (size_t)t * GMW + g * GMGD + 4 * kq; unsigned char* yrow = F.ws + SC_Y8 + (size_t)t * GMW + g * GMGD + 4 * kq;
.LBB0_323:
	s_lshl_b32 s10, s19, 4
	s_and_b32 s22, s10, 0xffffff80
	s_and_b32 s16, s19, 7
	s_lshl_b32 s24, s16, 9
	s_mov_b32 s25, s11
	v_lshl_add_u64 v[0:1], v[22:23], 0, s[24:25]
	s_lshl_b32 s24, s16, 10
	v_lshl_add_u64 v[2:3], v[24:25], 0, s[24:25]
	v_lshl_add_u64 v[4:5], v[26:27], 0, s[24:25]
	s_lshl_b32 s10, s16, 8
	global_load_dwordx4 v[176:179], v[2:3], off
	global_load_dwordx4 v[180:183], v[2:3], off offset:16
	global_load_dwordx4 v[184:187], v[4:5], off
	global_load_dwordx4 v[188:191], v[4:5], off offset:16
	v_ashrrev_i32_e32 v37, 5, v29
	v_add_u32_e32 v14, s22, v37
	v_ashrrev_i32_e32 v15, 31, v14
	v_lshlrev_b64 v[14:15], 12, v[14:15]
	v_lshl_add_u64 v[172:173], v[0:1], 0, v[14:15]
	s_mov_b32 s24, 0x10000
	global_load_dwordx4 v[140:143], v[172:173], off
	v_lshl_add_u64 v[172:173], v[172:173], 0, s[24:25]
	global_load_dwordx4 v[144:147], v[172:173], off
	v_lshl_add_u64 v[172:173], v[172:173], 0, s[24:25]
	global_load_dwordx4 v[148:151], v[172:173], off
	v_lshl_add_u64 v[172:173], v[172:173], 0, s[24:25]
	global_load_dwordx4 v[152:155], v[172:173], off
	v_lshl_add_u64 v[172:173], v[172:173], 0, s[24:25]
	global_load_dwordx4 v[156:159], v[172:173], off
	v_lshl_add_u64 v[172:173], v[172:173], 0, s[24:25]
	global_load_dwordx4 v[160:163], v[172:173], off
	v_lshl_add_u64 v[172:173], v[172:173], 0, s[24:25]
	global_load_dwordx4 v[164:167], v[172:173], off
	v_lshl_add_u64 v[172:173], v[172:173], 0, s[24:25]
	global_load_dwordx4 v[168:171], v[172:173], off
	v_lshl_add_u32 v20, s16, 7, v36
	v_lshlrev_b64 v[82:83], 8, v[20:21]
	v_lshl_add_u64 v[82:83], v[18:19], 0, v[82:83]
	v_lshl_add_u64 v[174:175], v[20:21], 2, s[8:9]
	global_load_dwordx2 v[84:85], v[82:83], off
	global_load_dwordx2 v[86:87], v[82:83], off offset:32
	global_load_dwordx2 v[88:89], v[82:83], off offset:64
	global_load_dwordx2 v[90:91], v[82:83], off offset:96
	global_load_dwordx2 v[92:93], v[82:83], off offset:128
	global_load_dwordx2 v[94:95], v[82:83], off offset:160
	global_load_dwordx2 v[96:97], v[82:83], off offset:192
	global_load_dwordx2 v[98:99], v[82:83], off offset:224
	global_load_dword v100, v[174:175], off
	v_add_u32_e32 v30, s22, v36
	v_ashrrev_i32_e32 v31, 31, v30
	v_lshlrev_b64 v[32:33], 12, v[30:31]
	v_lshl_add_u64 v[32:33], s[4:5], 0, v[32:33]
	s_lshl_b32 s24, s10, 1
	v_lshl_add_u64 v[32:33], v[32:33], 0, s[24:25]
	v_lshl_add_u64 v[102:103], v[16:17], 1, v[32:33]
	global_load_dwordx2 v[104:105], v[102:103], off
	global_load_dwordx2 v[106:107], v[102:103], off offset:32
	global_load_dwordx2 v[108:109], v[102:103], off offset:64
	global_load_dwordx2 v[110:111], v[102:103], off offset:96
	global_load_dwordx2 v[112:113], v[102:103], off offset:128
	global_load_dwordx2 v[114:115], v[102:103], off offset:160
	global_load_dwordx2 v[116:117], v[102:103], off offset:192
	global_load_dwordx2 v[118:119], v[102:103], off offset:224
	global_load_dwordx2 v[120:121], v[102:103], off offset:256
	global_load_dwordx2 v[122:123], v[102:103], off offset:288
	global_load_dwordx2 v[124:125], v[102:103], off offset:320
	global_load_dwordx2 v[126:127], v[102:103], off offset:352
	global_load_dwordx2 v[128:129], v[102:103], off offset:384
	global_load_dwordx2 v[130:131], v[102:103], off offset:416
	global_load_dwordx2 v[132:133], v[102:103], off offset:448
	global_load_dwordx2 v[134:135], v[102:103], off offset:480
	v_lshlrev_b64 v[30:31], 11, v[30:31]
	v_lshl_add_u64 v[30:31], s[12:13], 0, v[30:31]
	s_mov_b32 s24, s10
	v_lshl_add_u64 v[30:31], v[30:31], 0, s[24:25]
	v_lshl_add_u64 v[136:137], v[30:31], 0, v[16:17]
	s_and_saveexec_b64 s[16:17], vcc
	s_cbranch_execz .LBB0_325
	v_add_u32_e32 v0, s22, v29
	v_ashrrev_i32_e32 v1, 31, v0
	v_lshlrev_b64 v[0:1], 8, v[0:1]
	v_lshl_add_u64 v[78:79], s[6:7], 0, v[0:1]
	global_load_dwordx4 v[0:3], v[78:79], off
	global_load_dwordx4 v[4:7], v[78:79], off offset:16
	global_load_dwordx4 v[8:11], v[78:79], off offset:32
	global_load_dwordx4 v[12:15], v[78:79], off offset:48
	global_load_dwordx4 v[30:33], v[78:79], off offset:64
	global_load_dwordx4 v[38:41], v[78:79], off offset:80
	global_load_dwordx4 v[42:45], v[78:79], off offset:96
	global_load_dwordx4 v[46:49], v[78:79], off offset:112
	global_load_dwordx4 v[50:53], v[78:79], off offset:128
	global_load_dwordx4 v[54:57], v[78:79], off offset:144
	global_load_dwordx4 v[58:61], v[78:79], off offset:160
	global_load_dwordx4 v[62:65], v[78:79], off offset:176
	global_load_dwordx4 v[66:69], v[78:79], off offset:192
	global_load_dwordx4 v[70:73], v[78:79], off offset:208
	global_load_dwordx4 v[74:77], v[78:79], off offset:224
	s_nop 0
	global_load_dwordx4 v[78:81], v[78:79], off offset:240
	s_waitcnt vmcnt(15)
	v_pk_add_f32 v[0:1], v[0:1], v[2:3]
	s_waitcnt vmcnt(14)
	v_pk_add_f32 v[2:3], v[4:5], v[6:7]
	v_pk_add_f32 v[0:1], v[0:1], 0 op_sel_hi:[1,0]
	s_waitcnt vmcnt(13)
	v_pk_add_f32 v[4:5], v[8:9], v[10:11]
	v_pk_add_f32 v[0:1], v[0:1], v[2:3]
	s_waitcnt vmcnt(12)
	v_pk_add_f32 v[6:7], v[12:13], v[14:15]
	v_pk_add_f32 v[0:1], v[0:1], v[4:5]
	s_waitcnt vmcnt(11)
	v_pk_add_f32 v[8:9], v[30:31], v[32:33]
	v_pk_add_f32 v[0:1], v[0:1], v[6:7]
	s_waitcnt vmcnt(10)
	v_pk_add_f32 v[10:11], v[38:39], v[40:41]
	v_pk_add_f32 v[0:1], v[0:1], v[8:9]
	s_waitcnt vmcnt(9)
	v_pk_add_f32 v[12:13], v[42:43], v[44:45]
	v_pk_add_f32 v[0:1], v[0:1], v[10:11]
	s_waitcnt vmcnt(8)
	v_pk_add_f32 v[14:15], v[46:47], v[48:49]
	v_pk_add_f32 v[0:1], v[0:1], v[12:13]
	s_waitcnt vmcnt(7)
	v_pk_add_f32 v[30:31], v[50:51], v[52:53]
	v_pk_add_f32 v[0:1], v[0:1], v[14:15]
	s_waitcnt vmcnt(6)
	v_pk_add_f32 v[32:33], v[54:55], v[56:57]
	v_pk_add_f32 v[0:1], v[0:1], v[30:31]
	s_waitcnt vmcnt(5)
	v_pk_add_f32 v[38:39], v[58:59], v[60:61]
	v_pk_add_f32 v[0:1], v[0:1], v[32:33]
	s_waitcnt vmcnt(4)
	v_pk_add_f32 v[40:41], v[62:63], v[64:65]
	v_pk_add_f32 v[0:1], v[0:1], v[38:39]
	s_waitcnt vmcnt(3)
	v_pk_add_f32 v[42:43], v[66:67], v[68:69]
	v_pk_add_f32 v[0:1], v[0:1], v[40:41]
	s_waitcnt vmcnt(2)
	v_pk_add_f32 v[44:45], v[70:71], v[72:73]
	v_pk_add_f32 v[0:1], v[0:1], v[42:43]
	s_waitcnt vmcnt(1)
	v_pk_add_f32 v[46:47], v[74:75], v[76:77]
	v_pk_add_f32 v[0:1], v[0:1], v[44:45]
	s_waitcnt vmcnt(0)
	v_pk_add_f32 v[2:3], v[78:79], v[80:81]
	v_pk_add_f32 v[0:1], v[0:1], v[46:47]
	s_nop 0
	v_pk_add_f32 v[0:1], v[0:1], v[2:3]
	s_nop 0
	v_pk_mul_f32 v[0:1], v[0:1], s[14:15] op_sel_hi:[1,0]
	s_nop 0
	v_fma_f32 v1, -v0, v0, v1
	v_max_f32_e32 v1, 0, v1
	v_add_f32_e32 v1, 0x358637bd, v1
	v_rsq_f32_e32 v1, v1
	ds_write_b64 v35, v[0:1]
; #define GAS __attribute__((address_space(1)))
; #define LAS __attribute__((address_space(3)))
; __device__ __forceinline__ u32x4 pack8f(const f32x4 a, const f32x4 b) { u32x4 w; w.x = pk2(a[0], a[1]); w.y = pk2(a[2], a[3]); w.z = pk2(b[0], b[1]); w.w = pk2(b[2], b[3]); return w; }
; __device__ __forceinline__ void gating_phase(Frame& F) {
;     ...
;         __syncthreads();
; #pragma unroll 2
;         for (int i = 0; i < 8; ++i) { const int idx = F.tid + 512 * i, r = idx >> 5, ch = idx & 31;
;             const u32x4 raw = *(const GAS u32x4*)(V + (size_t)(row0 + r) * GMW + g * GMGD + ch * 8);
;             const f32x2 st = lst[r]; const float mean = st.x, rstd = st.y;
;             const f32x4 g0 = *(const f32x4*)(lng + g * GMGD + ch * 8), g1 = *(const f32x4*)(lng + g * GMGD + ch * 8 + 4), b0 = *(const f32x4*)(lnb + g * GMGD + ch * 8), b1 = *(const f32x4*)(lnb + g * GMGD + ch * 8 + 4);
;             f32x4 x0 = {bf_lo(raw.x), bf_hi(raw.x), bf_lo(raw.y), bf_hi(raw.y)}, x1 = {bf_lo(raw.z), bf_hi(raw.z), bf_lo(raw.w), bf_hi(raw.w)};
;             x0 = (x0 - mean) * rstd * g0 + b0; x1 = (x1 - mean) * rstd * g1 + b1;
;             *(LAS u32x4*)(vl + r * VSTG + ch * 16) = pack8f(x0, x1); }
.LBB0_325:
	s_or_b64 exec, exec, s[16:17]
	v_lshl_add_u32 v192, v37, 3, s18
	v_mad_u32_u24 v210, v37, s15, v28
	s_waitcnt lgkmcnt(0)
	s_barrier
	ds_read_b64 v[194:195], v192
	ds_read_b64 v[196:197], v192 offset:128
	ds_read_b64 v[198:199], v192 offset:256
	ds_read_b64 v[200:201], v192 offset:384
	ds_read_b64 v[202:203], v192 offset:512
	ds_read_b64 v[204:205], v192 offset:640
	ds_read_b64 v[206:207], v192 offset:768
	ds_read_b64 v[208:209], v192 offset:896
	s_waitcnt lgkmcnt(0)
	s_waitcnt vmcnt(32)
	v_lshlrev_b32_e32 v46, 16, v140
	v_and_b32_e32 v47, 0xffff0000, v140
	v_lshlrev_b32_e32 v38, 16, v141
	v_and_b32_e32 v39, 0xffff0000, v141
	v_lshlrev_b32_e32 v48, 16, v142
	v_and_b32_e32 v49, 0xffff0000, v142
	v_lshlrev_b32_e32 v52, 16, v143
	v_and_b32_e32 v53, 0xffff0000, v143
	v_sub_f32_e32 v39, v39, v194
	v_sub_f32_e32 v38, v38, v194
	v_sub_f32_e32 v41, v47, v194
	v_sub_f32_e32 v40, v46, v194
	v_sub_f32_e32 v47, v53, v194
	v_sub_f32_e32 v46, v52, v194
	v_sub_f32_e32 v49, v49, v194
	v_sub_f32_e32 v48, v48, v194
	v_pk_mul_f32 v[40:41], v[194:195], v[40:41] op_sel:[1,0]
	v_pk_mul_f32 v[38:39], v[194:195], v[38:39] op_sel:[1,0]
	v_pk_mul_f32 v[48:49], v[194:195], v[48:49] op_sel:[1,0]
	v_pk_mul_f32 v[50:51], v[194:195], v[46:47] op_sel:[1,0]
	v_pk_fma_f32 v[12:13], v[178:179], v[38:39], v[186:187]
	v_pk_fma_f32 v[10:11], v[176:177], v[40:41], v[184:185]
	v_pk_fma_f32 v[14:15], v[182:183], v[50:51], v[190:191]
	v_pk_fma_f32 v[8:9], v[180:181], v[48:49], v[188:189]
	v_cvt_pk_bf16_f32 v6, v10, v11
	v_cvt_pk_bf16_f32 v7, v12, v13
	v_cvt_pk_bf16_f32 v8, v8, v9
	v_cvt_pk_bf16_f32 v9, v14, v15
	ds_write_b128 v210, v[6:9]
	s_waitcnt vmcnt(31)
	v_lshlrev_b32_e32 v46, 16, v144
	v_and_b32_e32 v47, 0xffff0000, v144
	v_lshlrev_b32_e32 v38, 16, v145
	v_and_b32_e32 v39, 0xffff0000, v145
	v_lshlrev_b32_e32 v48, 16, v146
	v_and_b32_e32 v49, 0xffff0000, v146
	v_lshlrev_b32_e32 v52, 16, v147
	v_and_b32_e32 v53, 0xffff0000, v147
	v_sub_f32_e32 v39, v39, v196
	v_sub_f32_e32 v38, v38, v196
	v_sub_f32_e32 v41, v47, v196
	v_sub_f32_e32 v40, v46, v196
	v_sub_f32_e32 v47, v53, v196
	v_sub_f32_e32 v46, v52, v196
	v_sub_f32_e32 v49, v49, v196
	v_sub_f32_e32 v48, v48, v196
	v_pk_mul_f32 v[40:41], v[196:197], v[40:41] op_sel:[1,0]
	v_pk_mul_f32 v[38:39], v[196:197], v[38:39] op_sel:[1,0]
	v_pk_mul_f32 v[48:49], v[196:197], v[48:49] op_sel:[1,0]
	v_pk_mul_f32 v[50:51], v[196:197], v[46:47] op_sel:[1,0]
	v_pk_fma_f32 v[12:13], v[178:179], v[38:39], v[186:187]
	v_pk_fma_f32 v[10:11], v[176:177], v[40:41], v[184:185]
	v_pk_fma_f32 v[14:15], v[182:183], v[50:51], v[190:191]
	v_pk_fma_f32 v[8:9], v[180:181], v[48:49], v[188:189]
	v_cvt_pk_bf16_f32 v6, v10, v11
	v_cvt_pk_bf16_f32 v7, v12, v13
	v_cvt_pk_bf16_f32 v8, v8, v9
	v_cvt_pk_bf16_f32 v9, v14, v15
	ds_write_b128 v210, v[6:9] offset:8704
	s_waitcnt vmcnt(30)
	v_lshlrev_b32_e32 v46, 16, v148
	v_and_b32_e32 v47, 0xffff0000, v148
	v_lshlrev_b32_e32 v38, 16, v149
	v_and_b32_e32 v39, 0xffff0000, v149
	v_lshlrev_b32_e32 v48, 16, v150
	v_and_b32_e32 v49, 0xffff0000, v150
	v_lshlrev_b32_e32 v52, 16, v151
	v_and_b32_e32 v53, 0xffff0000, v151
	v_sub_f32_e32 v39, v39, v198
	v_sub_f32_e32 v38, v38, v198
	v_sub_f32_e32 v41, v47, v198
	v_sub_f32_e32 v40, v46, v198
	v_sub_f32_e32 v47, v53, v198
	v_sub_f32_e32 v46, v52, v198
	v_sub_f32_e32 v49, v49, v198
	v_sub_f32_e32 v48, v48, v198
	v_pk_mul_f32 v[40:41], v[198:199], v[40:41] op_sel:[1,0]
	v_pk_mul_f32 v[38:39], v[198:199], v[38:39] op_sel:[1,0]
	v_pk_mul_f32 v[48:49], v[198:199], v[48:49] op_sel:[1,0]
	v_pk_mul_f32 v[50:51], v[198:199], v[46:47] op_sel:[1,0]
	v_pk_fma_f32 v[12:13], v[178:179], v[38:39], v[186:187]
	v_pk_fma_f32 v[10:11], v[176:177], v[40:41], v[184:185]
	v_pk_fma_f32 v[14:15], v[182:183], v[50:51], v[190:191]
	v_pk_fma_f32 v[8:9], v[180:181], v[48:49], v[188:189]
	v_cvt_pk_bf16_f32 v6, v10, v11
	v_cvt_pk_bf16_f32 v7, v12, v13
	v_cvt_pk_bf16_f32 v8, v8, v9
	v_cvt_pk_bf16_f32 v9, v14, v15
	ds_write_b128 v210, v[6:9] offset:17408
	s_waitcnt vmcnt(29)
	v_lshlrev_b32_e32 v46, 16, v152
	v_and_b32_e32 v47, 0xffff0000, v152
	v_lshlrev_b32_e32 v38, 16, v153
	v_and_b32_e32 v39, 0xffff0000, v153
	v_lshlrev_b32_e32 v48, 16, v154
	v_and_b32_e32 v49, 0xffff0000, v154
	v_lshlrev_b32_e32 v52, 16, v155
	v_and_b32_e32 v53, 0xffff0000, v155
	v_sub_f32_e32 v39, v39, v200
	v_sub_f32_e32 v38, v38, v200
	v_sub_f32_e32 v41, v47, v200
	v_sub_f32_e32 v40, v46, v200
	v_sub_f32_e32 v47, v53, v200
	v_sub_f32_e32 v46, v52, v200
	v_sub_f32_e32 v49, v49, v200
	v_sub_f32_e32 v48, v48, v200
	v_pk_mul_f32 v[40:41], v[200:201], v[40:41] op_sel:[1,0]
	v_pk_mul_f32 v[38:39], v[200:201], v[38:39] op_sel:[1,0]
	v_pk_mul_f32 v[48:49], v[200:201], v[48:49] op_sel:[1,0]
	v_pk_mul_f32 v[50:51], v[200:201], v[46:47] op_sel:[1,0]
	v_pk_fma_f32 v[12:13], v[178:179], v[38:39], v[186:187]
	v_pk_fma_f32 v[10:11], v[176:177], v[40:41], v[184:185]
	v_pk_fma_f32 v[14:15], v[182:183], v[50:51], v[190:191]
	v_pk_fma_f32 v[8:9], v[180:181], v[48:49], v[188:189]
	v_cvt_pk_bf16_f32 v6, v10, v11
	v_cvt_pk_bf16_f32 v7, v12, v13
	v_cvt_pk_bf16_f32 v8, v8, v9
	v_cvt_pk_bf16_f32 v9, v14, v15
	ds_write_b128 v210, v[6:9] offset:26112
	s_waitcnt vmcnt(28)
; #define GAS __attribute__((address_space(1)))
; #define LAS __attribute__((address_space(3)))
; __device__ __forceinline__ u32x4 pack8f(const f32x4 a, const f32x4 b) { u32x4 w; w.x = pk2(a[0], a[1]); w.y = pk2(a[2], a[3]); w.z = pk2(b[0], b[1]); w.w = pk2(b[2], b[3]); return w; }
; __device__ __forceinline__ void gating_phase(Frame& F) {
;     ...
;         for (int i = 0; i < 8; ++i) { const int idx = F.tid + 512 * i, r = idx >> 5, ch = idx & 31;
;             const u32x4 raw = *(const GAS u32x4*)(V + (size_t)(row0 + r) * GMW + g * GMGD + ch * 8);
;             const f32x2 st = lst[r]; const float mean = st.x, rstd = st.y;
;             const f32x4 g0 = *(const f32x4*)(lng + g * GMGD + ch * 8), g1 = *(const f32x4*)(lng + g * GMGD + ch * 8 + 4), b0 = *(const f32x4*)(lnb + g * GMGD + ch * 8), b1 = *(const f32x4*)(lnb + g * GMGD + ch * 8 + 4);
;             f32x4 x0 = {bf_lo(raw.x), bf_hi(raw.x), bf_lo(raw.y), bf_hi(raw.y)}, x1 = {bf_lo(raw.z), bf_hi(raw.z), bf_lo(raw.w), bf_hi(raw.w)};
;             x0 = (x0 - mean) * rstd * g0 + b0; x1 = (x1 - mean) * rstd * g1 + b1;
;             *(LAS u32x4*)(vl + r * VSTG + ch * 16) = pack8f(x0, x1); }
;         __syncthreads();
	v_lshlrev_b32_e32 v46, 16, v156
	v_and_b32_e32 v47, 0xffff0000, v156
	v_lshlrev_b32_e32 v38, 16, v157
	v_and_b32_e32 v39, 0xffff0000, v157
	v_lshlrev_b32_e32 v48, 16, v158
	v_and_b32_e32 v49, 0xffff0000, v158
	v_lshlrev_b32_e32 v52, 16, v159
	v_and_b32_e32 v53, 0xffff0000, v159
	v_sub_f32_e32 v39, v39, v202
	v_sub_f32_e32 v38, v38, v202
	v_sub_f32_e32 v41, v47, v202
	v_sub_f32_e32 v40, v46, v202
	v_sub_f32_e32 v47, v53, v202
	v_sub_f32_e32 v46, v52, v202
	v_sub_f32_e32 v49, v49, v202
	v_sub_f32_e32 v48, v48, v202
	v_pk_mul_f32 v[40:41], v[202:203], v[40:41] op_sel:[1,0]
	v_pk_mul_f32 v[38:39], v[202:203], v[38:39] op_sel:[1,0]
	v_pk_mul_f32 v[48:49], v[202:203], v[48:49] op_sel:[1,0]
	v_pk_mul_f32 v[50:51], v[202:203], v[46:47] op_sel:[1,0]
	v_pk_fma_f32 v[12:13], v[178:179], v[38:39], v[186:187]
	v_pk_fma_f32 v[10:11], v[176:177], v[40:41], v[184:185]
	v_pk_fma_f32 v[14:15], v[182:183], v[50:51], v[190:191]
	v_pk_fma_f32 v[8:9], v[180:181], v[48:49], v[188:189]
	v_cvt_pk_bf16_f32 v6, v10, v11
	v_cvt_pk_bf16_f32 v7, v12, v13
	v_cvt_pk_bf16_f32 v8, v8, v9
	v_cvt_pk_bf16_f32 v9, v14, v15
	ds_write_b128 v210, v[6:9] offset:34816
	s_waitcnt vmcnt(27)
	v_lshlrev_b32_e32 v46, 16, v160
	v_and_b32_e32 v47, 0xffff0000, v160
	v_lshlrev_b32_e32 v38, 16, v161
	v_and_b32_e32 v39, 0xffff0000, v161
	v_lshlrev_b32_e32 v48, 16, v162
	v_and_b32_e32 v49, 0xffff0000, v162
	v_lshlrev_b32_e32 v52, 16, v163
	v_and_b32_e32 v53, 0xffff0000, v163
	v_sub_f32_e32 v39, v39, v204
	v_sub_f32_e32 v38, v38, v204
	v_sub_f32_e32 v41, v47, v204
	v_sub_f32_e32 v40, v46, v204
	v_sub_f32_e32 v47, v53, v204
	v_sub_f32_e32 v46, v52, v204
	v_sub_f32_e32 v49, v49, v204
	v_sub_f32_e32 v48, v48, v204
	v_pk_mul_f32 v[40:41], v[204:205], v[40:41] op_sel:[1,0]
	v_pk_mul_f32 v[38:39], v[204:205], v[38:39] op_sel:[1,0]
	v_pk_mul_f32 v[48:49], v[204:205], v[48:49] op_sel:[1,0]
	v_pk_mul_f32 v[50:51], v[204:205], v[46:47] op_sel:[1,0]
	v_pk_fma_f32 v[12:13], v[178:179], v[38:39], v[186:187]
	v_pk_fma_f32 v[10:11], v[176:177], v[40:41], v[184:185]
	v_pk_fma_f32 v[14:15], v[182:183], v[50:51], v[190:191]
	v_pk_fma_f32 v[8:9], v[180:181], v[48:49], v[188:189]
	v_cvt_pk_bf16_f32 v6, v10, v11
	v_cvt_pk_bf16_f32 v7, v12, v13
	v_cvt_pk_bf16_f32 v8, v8, v9
	v_cvt_pk_bf16_f32 v9, v14, v15
	ds_write_b128 v210, v[6:9] offset:43520
	s_waitcnt vmcnt(26)
	v_lshlrev_b32_e32 v46, 16, v164
	v_and_b32_e32 v47, 0xffff0000, v164
	v_lshlrev_b32_e32 v38, 16, v165
	v_and_b32_e32 v39, 0xffff0000, v165
	v_lshlrev_b32_e32 v48, 16, v166
	v_and_b32_e32 v49, 0xffff0000, v166
	v_lshlrev_b32_e32 v52, 16, v167
	v_and_b32_e32 v53, 0xffff0000, v167
	v_sub_f32_e32 v39, v39, v206
	v_sub_f32_e32 v38, v38, v206
	v_sub_f32_e32 v41, v47, v206
	v_sub_f32_e32 v40, v46, v206
	v_sub_f32_e32 v47, v53, v206
	v_sub_f32_e32 v46, v52, v206
	v_sub_f32_e32 v49, v49, v206
	v_sub_f32_e32 v48, v48, v206
	v_pk_mul_f32 v[40:41], v[206:207], v[40:41] op_sel:[1,0]
	v_pk_mul_f32 v[38:39], v[206:207], v[38:39] op_sel:[1,0]
	v_pk_mul_f32 v[48:49], v[206:207], v[48:49] op_sel:[1,0]
	v_pk_mul_f32 v[50:51], v[206:207], v[46:47] op_sel:[1,0]
	v_pk_fma_f32 v[12:13], v[178:179], v[38:39], v[186:187]
	v_pk_fma_f32 v[10:11], v[176:177], v[40:41], v[184:185]
	v_pk_fma_f32 v[14:15], v[182:183], v[50:51], v[190:191]
	v_pk_fma_f32 v[8:9], v[180:181], v[48:49], v[188:189]
	v_cvt_pk_bf16_f32 v6, v10, v11
	v_cvt_pk_bf16_f32 v7, v12, v13
	v_cvt_pk_bf16_f32 v8, v8, v9
	v_cvt_pk_bf16_f32 v9, v14, v15
	ds_write_b128 v210, v[6:9] offset:52224
	s_waitcnt vmcnt(25)
	v_lshlrev_b32_e32 v46, 16, v168
	v_and_b32_e32 v47, 0xffff0000, v168
	v_lshlrev_b32_e32 v38, 16, v169
	v_and_b32_e32 v39, 0xffff0000, v169
	v_lshlrev_b32_e32 v48, 16, v170
	v_and_b32_e32 v49, 0xffff0000, v170
	v_lshlrev_b32_e32 v52, 16, v171
	v_and_b32_e32 v53, 0xffff0000, v171
	v_sub_f32_e32 v39, v39, v208
	v_sub_f32_e32 v38, v38, v208
	v_sub_f32_e32 v41, v47, v208
	v_sub_f32_e32 v40, v46, v208
	v_sub_f32_e32 v47, v53, v208
	v_sub_f32_e32 v46, v52, v208
	v_sub_f32_e32 v49, v49, v208
	v_sub_f32_e32 v48, v48, v208
	v_pk_mul_f32 v[40:41], v[208:209], v[40:41] op_sel:[1,0]
	v_pk_mul_f32 v[38:39], v[208:209], v[38:39] op_sel:[1,0]
	v_pk_mul_f32 v[48:49], v[208:209], v[48:49] op_sel:[1,0]
	v_pk_mul_f32 v[50:51], v[208:209], v[46:47] op_sel:[1,0]
	v_pk_fma_f32 v[12:13], v[178:179], v[38:39], v[186:187]
	v_pk_fma_f32 v[10:11], v[176:177], v[40:41], v[184:185]
	v_pk_fma_f32 v[14:15], v[182:183], v[50:51], v[190:191]
	v_pk_fma_f32 v[8:9], v[180:181], v[48:49], v[188:189]
	v_cvt_pk_bf16_f32 v6, v10, v11
	v_cvt_pk_bf16_f32 v7, v12, v13
	v_cvt_pk_bf16_f32 v8, v8, v9
	v_cvt_pk_bf16_f32 v9, v14, v15
	ds_write_b128 v210, v[6:9] offset:60928
	s_waitcnt lgkmcnt(0)
	s_barrier
; __device__ __forceinline__ void gating_phase(Frame& F) {
;     ...
;         GT_DT(0); GT_DT(1); GT_DT(2); GT_DT(3); GT_DT(4); GT_DT(5); GT_DT(6); GT_DT(7); GT_DT(8); GT_DT(9); GT_DT(10); GT_DT(11); GT_DT(12); GT_DT(13); GT_DT(14); GT_DT(15);
	ds_read_b64_tr_b16 v[38:39], v34 offset:0
	ds_read_b64_tr_b16 v[40:41], v34 offset:8704
	ds_read_b64_tr_b16 v[42:43], v34 offset:17408
	ds_read_b64_tr_b16 v[44:45], v34 offset:26112
	ds_read_b64_tr_b16 v[46:47], v34 offset:34816
	ds_read_b64_tr_b16 v[48:49], v34 offset:43520
	ds_read_b64_tr_b16 v[50:51], v34 offset:52224
	ds_read_b64_tr_b16 v[52:53], v34 offset:60928
	s_waitcnt lgkmcnt(0)
	s_waitcnt vmcnt(17)
	v_mfma_f32_16x16x32_bf16 v[38:41], v[38:41], v[84:87], 0
	s_waitcnt vmcnt(15)
	v_lshlrev_b32_e32 v37, 16, v104
	v_mul_f32_e32 v37, 0x41000000, v37
	v_mfma_f32_16x16x32_bf16 v[38:41], v[42:45], v[88:91], v[38:41]
	v_and_b32_e32 v42, 0xffff0000, v104
	v_lshlrev_b32_e32 v43, 16, v105
	v_mul_f32_e32 v42, 0x41000000, v42
	v_mfma_f32_16x16x32_bf16 v[38:41], v[46:49], v[92:95], v[38:41]
	v_mul_f32_e32 v43, 0x41000000, v43
	v_and_b32_e32 v44, 0xffff0000, v105
	v_mfma_f32_16x16x32_bf16 v[38:41], v[50:53], v[96:99], v[38:41]
	s_nop 7
	v_add_f32_e32 v38, v100, v38
	v_add_f32_e32 v39, v100, v39
	v_add_f32_e32 v40, v100, v40
	v_mul_f32_e32 v37, v37, v38
	v_mul_f32_e32 v38, v42, v39
	v_mul_f32_e32 v39, v43, v40
	v_mov_b32_e32 v40, v21
	v_cvt_pk_fp8_f32 v40, v37, v38
	v_mul_f32_e32 v37, 0x41000000, v44
	v_add_f32_e32 v38, v100, v41
	v_mul_f32_e32 v37, v37, v38
	v_cvt_pk_fp8_f32 v40, v39, v37 op_sel:[0,0,1]
	global_store_dword v[136:137], v40, off
	ds_read_b64_tr_b16 v[38:39], v34 offset:32
	ds_read_b64_tr_b16 v[40:41], v34 offset:8736
	ds_read_b64_tr_b16 v[42:43], v34 offset:17440
	ds_read_b64_tr_b16 v[44:45], v34 offset:26144
	ds_read_b64_tr_b16 v[46:47], v34 offset:34848
	ds_read_b64_tr_b16 v[48:49], v34 offset:43552
	ds_read_b64_tr_b16 v[50:51], v34 offset:52256
	ds_read_b64_tr_b16 v[52:53], v34 offset:60960
	s_waitcnt lgkmcnt(0)
	v_mfma_f32_16x16x32_bf16 v[38:41], v[38:41], v[84:87], 0
	s_waitcnt vmcnt(15)
	v_lshlrev_b32_e32 v37, 16, v106
	v_mul_f32_e32 v37, 0x41000000, v37
	v_mfma_f32_16x16x32_bf16 v[38:41], v[42:45], v[88:91], v[38:41]
	v_and_b32_e32 v42, 0xffff0000, v106
	v_lshlrev_b32_e32 v43, 16, v107
	v_mul_f32_e32 v42, 0x41000000, v42
	v_mfma_f32_16x16x32_bf16 v[38:41], v[46:49], v[92:95], v[38:41]
	v_mul_f32_e32 v43, 0x41000000, v43
	v_and_b32_e32 v44, 0xffff0000, v107
	v_mfma_f32_16x16x32_bf16 v[38:41], v[50:53], v[96:99], v[38:41]
	s_nop 7
	v_add_f32_e32 v38, v100, v38
	v_add_f32_e32 v39, v100, v39
	v_add_f32_e32 v40, v100, v40
	v_mul_f32_e32 v37, v37, v38
	v_mul_f32_e32 v38, v42, v39
	v_mul_f32_e32 v39, v43, v40
	v_mov_b32_e32 v40, v21
	v_cvt_pk_fp8_f32 v40, v37, v38
	v_mul_f32_e32 v37, 0x41000000, v44
	v_add_f32_e32 v38, v100, v41
	v_mul_f32_e32 v37, v37, v38
	v_cvt_pk_fp8_f32 v40, v39, v37 op_sel:[0,0,1]
	global_store_dword v[136:137], v40, off offset:16
	ds_read_b64_tr_b16 v[38:39], v34 offset:64
	ds_read_b64_tr_b16 v[40:41], v34 offset:8768
	ds_read_b64_tr_b16 v[42:43], v34 offset:17472
	ds_read_b64_tr_b16 v[44:45], v34 offset:26176
	ds_read_b64_tr_b16 v[46:47], v34 offset:34880
	ds_read_b64_tr_b16 v[48:49], v34 offset:43584
	ds_read_b64_tr_b16 v[50:51], v34 offset:52288
	ds_read_b64_tr_b16 v[52:53], v34 offset:60992
	s_waitcnt lgkmcnt(0)
	v_mfma_f32_16x16x32_bf16 v[38:41], v[38:41], v[84:87], 0
	s_waitcnt vmcnt(15)
	v_lshlrev_b32_e32 v37, 16, v108
	v_mul_f32_e32 v37, 0x41000000, v37
	v_mfma_f32_16x16x32_bf16 v[38:41], v[42:45], v[88:91], v[38:41]
	v_and_b32_e32 v42, 0xffff0000, v108
	v_lshlrev_b32_e32 v43, 16, v109
	v_mul_f32_e32 v42, 0x41000000, v42
	v_mfma_f32_16x16x32_bf16 v[38:41], v[46:49], v[92:95], v[38:41]
	v_mul_f32_e32 v43, 0x41000000, v43
	v_and_b32_e32 v44, 0xffff0000, v109
	v_mfma_f32_16x16x32_bf16 v[38:41], v[50:53], v[96:99], v[38:41]
	s_nop 7
	v_add_f32_e32 v38, v100, v38
	v_add_f32_e32 v39, v100, v39
	v_add_f32_e32 v40, v100, v40
	v_mul_f32_e32 v37, v37, v38
	v_mul_f32_e32 v38, v42, v39
	v_mul_f32_e32 v39, v43, v40
	v_mov_b32_e32 v40, v21
	v_cvt_pk_fp8_f32 v40, v37, v38
	v_mul_f32_e32 v37, 0x41000000, v44
	v_add_f32_e32 v38, v100, v41
	v_mul_f32_e32 v37, v37, v38
	v_cvt_pk_fp8_f32 v40, v39, v37 op_sel:[0,0,1]
	global_store_dword v[136:137], v40, off offset:32
	ds_read_b64_tr_b16 v[38:39], v34 offset:96
	ds_read_b64_tr_b16 v[40:41], v34 offset:8800
	ds_read_b64_tr_b16 v[42:43], v34 offset:17504
	ds_read_b64_tr_b16 v[44:45], v34 offset:26208
	ds_read_b64_tr_b16 v[46:47], v34 offset:34912
	ds_read_b64_tr_b16 v[48:49], v34 offset:43616
	ds_read_b64_tr_b16 v[50:51], v34 offset:52320
	ds_read_b64_tr_b16 v[52:53], v34 offset:61024
	s_waitcnt lgkmcnt(0)
	v_mfma_f32_16x16x32_bf16 v[38:41], v[38:41], v[84:87], 0
	s_waitcnt vmcnt(15)
	v_lshlrev_b32_e32 v37, 16, v110
	v_mul_f32_e32 v37, 0x41000000, v37
	v_mfma_f32_16x16x32_bf16 v[38:41], v[42:45], v[88:91], v[38:41]
	v_and_b32_e32 v42, 0xffff0000, v110
	v_lshlrev_b32_e32 v43, 16, v111
	v_mul_f32_e32 v42, 0x41000000, v42
	v_mfma_f32_16x16x32_bf16 v[38:41], v[46:49], v[92:95], v[38:41]
	v_mul_f32_e32 v43, 0x41000000, v43
	v_and_b32_e32 v44, 0xffff0000, v111
	v_mfma_f32_16x16x32_bf16 v[38:41], v[50:53], v[96:99], v[38:41]
	s_nop 7
	v_add_f32_e32 v38, v100, v38
	v_add_f32_e32 v39, v100, v39
	v_add_f32_e32 v40, v100, v40
	v_mul_f32_e32 v37, v37, v38
	v_mul_f32_e32 v38, v42, v39
	v_mul_f32_e32 v39, v43, v40
	v_mov_b32_e32 v40, v21
	v_cvt_pk_fp8_f32 v40, v37, v38
	v_mul_f32_e32 v37, 0x41000000, v44
	v_add_f32_e32 v38, v100, v41
	v_mul_f32_e32 v37, v37, v38
	v_cvt_pk_fp8_f32 v40, v39, v37 op_sel:[0,0,1]
	global_store_dword v[136:137], v40, off offset:48
	ds_read_b64_tr_b16 v[38:39], v34 offset:128
	ds_read_b64_tr_b16 v[40:41], v34 offset:8832
	ds_read_b64_tr_b16 v[42:43], v34 offset:17536
	ds_read_b64_tr_b16 v[44:45], v34 offset:26240
	ds_read_b64_tr_b16 v[46:47], v34 offset:34944
	ds_read_b64_tr_b16 v[48:49], v34 offset:43648
	ds_read_b64_tr_b16 v[50:51], v34 offset:52352
	ds_read_b64_tr_b16 v[52:53], v34 offset:61056
	s_waitcnt lgkmcnt(0)
; __device__ __forceinline__ void gating_phase(Frame& F) {
;     ...
;         GT_DT(0); GT_DT(1); GT_DT(2); GT_DT(3); GT_DT(4); GT_DT(5); GT_DT(6); GT_DT(7); GT_DT(8); GT_DT(9); GT_DT(10); GT_DT(11); GT_DT(12); GT_DT(13); GT_DT(14); GT_DT(15);
	v_mfma_f32_16x16x32_bf16 v[38:41], v[38:41], v[84:87], 0
	s_waitcnt vmcnt(15)
	v_lshlrev_b32_e32 v37, 16, v112
	v_mul_f32_e32 v37, 0x41000000, v37
	v_mfma_f32_16x16x32_bf16 v[38:41], v[42:45], v[88:91], v[38:41]
	v_and_b32_e32 v42, 0xffff0000, v112
	v_lshlrev_b32_e32 v43, 16, v113
	v_mul_f32_e32 v42, 0x41000000, v42
	v_mfma_f32_16x16x32_bf16 v[38:41], v[46:49], v[92:95], v[38:41]
	v_mul_f32_e32 v43, 0x41000000, v43
	v_and_b32_e32 v44, 0xffff0000, v113
	v_mfma_f32_16x16x32_bf16 v[38:41], v[50:53], v[96:99], v[38:41]
	s_nop 7
	v_add_f32_e32 v38, v100, v38
	v_add_f32_e32 v39, v100, v39
	v_add_f32_e32 v40, v100, v40
	v_mul_f32_e32 v37, v37, v38
	v_mul_f32_e32 v38, v42, v39
	v_mul_f32_e32 v39, v43, v40
	v_mov_b32_e32 v40, v21
	v_cvt_pk_fp8_f32 v40, v37, v38
	v_mul_f32_e32 v37, 0x41000000, v44
	v_add_f32_e32 v38, v100, v41
	v_mul_f32_e32 v37, v37, v38
	v_cvt_pk_fp8_f32 v40, v39, v37 op_sel:[0,0,1]
	global_store_dword v[136:137], v40, off offset:64
	ds_read_b64_tr_b16 v[38:39], v34 offset:160
	ds_read_b64_tr_b16 v[40:41], v34 offset:8864
	ds_read_b64_tr_b16 v[42:43], v34 offset:17568
	ds_read_b64_tr_b16 v[44:45], v34 offset:26272
	ds_read_b64_tr_b16 v[46:47], v34 offset:34976
	ds_read_b64_tr_b16 v[48:49], v34 offset:43680
	ds_read_b64_tr_b16 v[50:51], v34 offset:52384
	ds_read_b64_tr_b16 v[52:53], v34 offset:61088
	s_waitcnt lgkmcnt(0)
	v_mfma_f32_16x16x32_bf16 v[38:41], v[38:41], v[84:87], 0
	s_waitcnt vmcnt(15)
	v_lshlrev_b32_e32 v37, 16, v114
	v_mul_f32_e32 v37, 0x41000000, v37
	v_mfma_f32_16x16x32_bf16 v[38:41], v[42:45], v[88:91], v[38:41]
	v_and_b32_e32 v42, 0xffff0000, v114
	v_lshlrev_b32_e32 v43, 16, v115
	v_mul_f32_e32 v42, 0x41000000, v42
	v_mfma_f32_16x16x32_bf16 v[38:41], v[46:49], v[92:95], v[38:41]
	v_mul_f32_e32 v43, 0x41000000, v43
	v_and_b32_e32 v44, 0xffff0000, v115
	v_mfma_f32_16x16x32_bf16 v[38:41], v[50:53], v[96:99], v[38:41]
	s_nop 7
	v_add_f32_e32 v38, v100, v38
	v_add_f32_e32 v39, v100, v39
	v_add_f32_e32 v40, v100, v40
	v_mul_f32_e32 v37, v37, v38
	v_mul_f32_e32 v38, v42, v39
	v_mul_f32_e32 v39, v43, v40
	v_mov_b32_e32 v40, v21
	v_cvt_pk_fp8_f32 v40, v37, v38
	v_mul_f32_e32 v37, 0x41000000, v44
	v_add_f32_e32 v38, v100, v41
	v_mul_f32_e32 v37, v37, v38
	v_cvt_pk_fp8_f32 v40, v39, v37 op_sel:[0,0,1]
	global_store_dword v[136:137], v40, off offset:80
	ds_read_b64_tr_b16 v[38:39], v34 offset:192
	ds_read_b64_tr_b16 v[40:41], v34 offset:8896
	ds_read_b64_tr_b16 v[42:43], v34 offset:17600
	ds_read_b64_tr_b16 v[44:45], v34 offset:26304
	ds_read_b64_tr_b16 v[46:47], v34 offset:35008
	ds_read_b64_tr_b16 v[48:49], v34 offset:43712
	ds_read_b64_tr_b16 v[50:51], v34 offset:52416
	ds_read_b64_tr_b16 v[52:53], v34 offset:61120
	s_waitcnt lgkmcnt(0)
	v_mfma_f32_16x16x32_bf16 v[38:41], v[38:41], v[84:87], 0
	s_waitcnt vmcnt(15)
	v_lshlrev_b32_e32 v37, 16, v116
	v_mul_f32_e32 v37, 0x41000000, v37
	v_mfma_f32_16x16x32_bf16 v[38:41], v[42:45], v[88:91], v[38:41]
	v_and_b32_e32 v42, 0xffff0000, v116
	v_lshlrev_b32_e32 v43, 16, v117
	v_mul_f32_e32 v42, 0x41000000, v42
	v_mfma_f32_16x16x32_bf16 v[38:41], v[46:49], v[92:95], v[38:41]
	v_mul_f32_e32 v43, 0x41000000, v43
	v_and_b32_e32 v44, 0xffff0000, v117
	v_mfma_f32_16x16x32_bf16 v[38:41], v[50:53], v[96:99], v[38:41]
	s_nop 7
	v_add_f32_e32 v38, v100, v38
	v_add_f32_e32 v39, v100, v39
	v_add_f32_e32 v40, v100, v40
	v_mul_f32_e32 v37, v37, v38
	v_mul_f32_e32 v38, v42, v39
	v_mul_f32_e32 v39, v43, v40
	v_mov_b32_e32 v40, v21
	v_cvt_pk_fp8_f32 v40, v37, v38
	v_mul_f32_e32 v37, 0x41000000, v44
	v_add_f32_e32 v38, v100, v41
	v_mul_f32_e32 v37, v37, v38
	v_cvt_pk_fp8_f32 v40, v39, v37 op_sel:[0,0,1]
	global_store_dword v[136:137], v40, off offset:96
	ds_read_b64_tr_b16 v[38:39], v34 offset:224
	ds_read_b64_tr_b16 v[40:41], v34 offset:8928
	ds_read_b64_tr_b16 v[42:43], v34 offset:17632
	ds_read_b64_tr_b16 v[44:45], v34 offset:26336
	ds_read_b64_tr_b16 v[46:47], v34 offset:35040
	ds_read_b64_tr_b16 v[48:49], v34 offset:43744
	ds_read_b64_tr_b16 v[50:51], v34 offset:52448
	ds_read_b64_tr_b16 v[52:53], v34 offset:61152
	s_waitcnt lgkmcnt(0)
	v_mfma_f32_16x16x32_bf16 v[38:41], v[38:41], v[84:87], 0
	s_waitcnt vmcnt(15)
	v_lshlrev_b32_e32 v37, 16, v118
	v_mul_f32_e32 v37, 0x41000000, v37
	v_mfma_f32_16x16x32_bf16 v[38:41], v[42:45], v[88:91], v[38:41]
	v_and_b32_e32 v42, 0xffff0000, v118
	v_lshlrev_b32_e32 v43, 16, v119
	v_mul_f32_e32 v42, 0x41000000, v42
	v_mfma_f32_16x16x32_bf16 v[38:41], v[46:49], v[92:95], v[38:41]
	v_mul_f32_e32 v43, 0x41000000, v43
	v_and_b32_e32 v44, 0xffff0000, v119
	v_mfma_f32_16x16x32_bf16 v[38:41], v[50:53], v[96:99], v[38:41]
	s_nop 7
	v_add_f32_e32 v38, v100, v38
	v_add_f32_e32 v39, v100, v39
	v_add_f32_e32 v40, v100, v40
	v_mul_f32_e32 v37, v37, v38
	v_mul_f32_e32 v38, v42, v39
	v_mul_f32_e32 v39, v43, v40
	v_mov_b32_e32 v40, v21
	v_cvt_pk_fp8_f32 v40, v37, v38
	v_mul_f32_e32 v37, 0x41000000, v44
	v_add_f32_e32 v38, v100, v41
	v_mul_f32_e32 v37, v37, v38
	v_cvt_pk_fp8_f32 v40, v39, v37 op_sel:[0,0,1]
	global_store_dword v[136:137], v40, off offset:112
	ds_read_b64_tr_b16 v[38:39], v34 offset:256
	ds_read_b64_tr_b16 v[40:41], v34 offset:8960
	ds_read_b64_tr_b16 v[42:43], v34 offset:17664
	ds_read_b64_tr_b16 v[44:45], v34 offset:26368
	ds_read_b64_tr_b16 v[46:47], v34 offset:35072
	ds_read_b64_tr_b16 v[48:49], v34 offset:43776
	ds_read_b64_tr_b16 v[50:51], v34 offset:52480
	ds_read_b64_tr_b16 v[52:53], v34 offset:61184
	s_waitcnt lgkmcnt(0)
	v_mfma_f32_16x16x32_bf16 v[38:41], v[38:41], v[84:87], 0
	s_waitcnt vmcnt(15)
; __device__ __forceinline__ void gating_phase(Frame& F) {
;     ...
;         GT_DT(0); GT_DT(1); GT_DT(2); GT_DT(3); GT_DT(4); GT_DT(5); GT_DT(6); GT_DT(7); GT_DT(8); GT_DT(9); GT_DT(10); GT_DT(11); GT_DT(12); GT_DT(13); GT_DT(14); GT_DT(15);
	v_lshlrev_b32_e32 v37, 16, v120
	v_mul_f32_e32 v37, 0x41000000, v37
	v_mfma_f32_16x16x32_bf16 v[38:41], v[42:45], v[88:91], v[38:41]
	v_and_b32_e32 v42, 0xffff0000, v120
	v_lshlrev_b32_e32 v43, 16, v121
	v_mul_f32_e32 v42, 0x41000000, v42
	v_mfma_f32_16x16x32_bf16 v[38:41], v[46:49], v[92:95], v[38:41]
	v_mul_f32_e32 v43, 0x41000000, v43
	v_and_b32_e32 v44, 0xffff0000, v121
	v_mfma_f32_16x16x32_bf16 v[38:41], v[50:53], v[96:99], v[38:41]
	s_nop 7
	v_add_f32_e32 v38, v100, v38
	v_add_f32_e32 v39, v100, v39
	v_add_f32_e32 v40, v100, v40
	v_mul_f32_e32 v37, v37, v38
	v_mul_f32_e32 v38, v42, v39
	v_mul_f32_e32 v39, v43, v40
	v_mov_b32_e32 v40, v21
	v_cvt_pk_fp8_f32 v40, v37, v38
	v_mul_f32_e32 v37, 0x41000000, v44
	v_add_f32_e32 v38, v100, v41
	v_mul_f32_e32 v37, v37, v38
	v_cvt_pk_fp8_f32 v40, v39, v37 op_sel:[0,0,1]
	global_store_dword v[136:137], v40, off offset:128
	ds_read_b64_tr_b16 v[38:39], v34 offset:288
	ds_read_b64_tr_b16 v[40:41], v34 offset:8992
	ds_read_b64_tr_b16 v[42:43], v34 offset:17696
	ds_read_b64_tr_b16 v[44:45], v34 offset:26400
	ds_read_b64_tr_b16 v[46:47], v34 offset:35104
	ds_read_b64_tr_b16 v[48:49], v34 offset:43808
	ds_read_b64_tr_b16 v[50:51], v34 offset:52512
	ds_read_b64_tr_b16 v[52:53], v34 offset:61216
	s_waitcnt lgkmcnt(0)
	v_mfma_f32_16x16x32_bf16 v[38:41], v[38:41], v[84:87], 0
	s_waitcnt vmcnt(15)
	v_lshlrev_b32_e32 v37, 16, v122
	v_mul_f32_e32 v37, 0x41000000, v37
	v_mfma_f32_16x16x32_bf16 v[38:41], v[42:45], v[88:91], v[38:41]
	v_and_b32_e32 v42, 0xffff0000, v122
	v_lshlrev_b32_e32 v43, 16, v123
	v_mul_f32_e32 v42, 0x41000000, v42
	v_mfma_f32_16x16x32_bf16 v[38:41], v[46:49], v[92:95], v[38:41]
	v_mul_f32_e32 v43, 0x41000000, v43
	v_and_b32_e32 v44, 0xffff0000, v123
	v_mfma_f32_16x16x32_bf16 v[38:41], v[50:53], v[96:99], v[38:41]
	s_nop 7
	v_add_f32_e32 v38, v100, v38
	v_add_f32_e32 v39, v100, v39
	v_add_f32_e32 v40, v100, v40
	v_mul_f32_e32 v37, v37, v38
	v_mul_f32_e32 v38, v42, v39
	v_mul_f32_e32 v39, v43, v40
	v_mov_b32_e32 v40, v21
	v_cvt_pk_fp8_f32 v40, v37, v38
	v_mul_f32_e32 v37, 0x41000000, v44
	v_add_f32_e32 v38, v100, v41
	v_mul_f32_e32 v37, v37, v38
	v_cvt_pk_fp8_f32 v40, v39, v37 op_sel:[0,0,1]
	global_store_dword v[136:137], v40, off offset:144
	ds_read_b64_tr_b16 v[38:39], v34 offset:320
	ds_read_b64_tr_b16 v[40:41], v34 offset:9024
	ds_read_b64_tr_b16 v[42:43], v34 offset:17728
	ds_read_b64_tr_b16 v[44:45], v34 offset:26432
	ds_read_b64_tr_b16 v[46:47], v34 offset:35136
	ds_read_b64_tr_b16 v[48:49], v34 offset:43840
	ds_read_b64_tr_b16 v[50:51], v34 offset:52544
	ds_read_b64_tr_b16 v[52:53], v34 offset:61248
	s_waitcnt lgkmcnt(0)
	v_mfma_f32_16x16x32_bf16 v[38:41], v[38:41], v[84:87], 0
	s_waitcnt vmcnt(15)
	v_lshlrev_b32_e32 v37, 16, v124
	v_mul_f32_e32 v37, 0x41000000, v37
	v_mfma_f32_16x16x32_bf16 v[38:41], v[42:45], v[88:91], v[38:41]
	v_and_b32_e32 v42, 0xffff0000, v124
	v_lshlrev_b32_e32 v43, 16, v125
	v_mul_f32_e32 v42, 0x41000000, v42
	v_mfma_f32_16x16x32_bf16 v[38:41], v[46:49], v[92:95], v[38:41]
	v_mul_f32_e32 v43, 0x41000000, v43
	v_and_b32_e32 v44, 0xffff0000, v125
	v_mfma_f32_16x16x32_bf16 v[38:41], v[50:53], v[96:99], v[38:41]
	s_nop 7
	v_add_f32_e32 v38, v100, v38
	v_add_f32_e32 v39, v100, v39
	v_add_f32_e32 v40, v100, v40
	v_mul_f32_e32 v37, v37, v38
	v_mul_f32_e32 v38, v42, v39
	v_mul_f32_e32 v39, v43, v40
	v_mov_b32_e32 v40, v21
	v_cvt_pk_fp8_f32 v40, v37, v38
	v_mul_f32_e32 v37, 0x41000000, v44
	v_add_f32_e32 v38, v100, v41
	v_mul_f32_e32 v37, v37, v38
	v_cvt_pk_fp8_f32 v40, v39, v37 op_sel:[0,0,1]
	global_store_dword v[136:137], v40, off offset:160
	ds_read_b64_tr_b16 v[38:39], v34 offset:352
	ds_read_b64_tr_b16 v[40:41], v34 offset:9056
	ds_read_b64_tr_b16 v[42:43], v34 offset:17760
	ds_read_b64_tr_b16 v[44:45], v34 offset:26464
	ds_read_b64_tr_b16 v[46:47], v34 offset:35168
	ds_read_b64_tr_b16 v[48:49], v34 offset:43872
	ds_read_b64_tr_b16 v[50:51], v34 offset:52576
	ds_read_b64_tr_b16 v[52:53], v34 offset:61280
	s_waitcnt lgkmcnt(0)
	v_mfma_f32_16x16x32_bf16 v[38:41], v[38:41], v[84:87], 0
	s_waitcnt vmcnt(15)
	v_lshlrev_b32_e32 v37, 16, v126
	v_mul_f32_e32 v37, 0x41000000, v37
	v_mfma_f32_16x16x32_bf16 v[38:41], v[42:45], v[88:91], v[38:41]
	v_and_b32_e32 v42, 0xffff0000, v126
	v_lshlrev_b32_e32 v43, 16, v127
	v_mul_f32_e32 v42, 0x41000000, v42
	v_mfma_f32_16x16x32_bf16 v[38:41], v[46:49], v[92:95], v[38:41]
	v_mul_f32_e32 v43, 0x41000000, v43
	v_and_b32_e32 v44, 0xffff0000, v127
	v_mfma_f32_16x16x32_bf16 v[38:41], v[50:53], v[96:99], v[38:41]
	s_nop 7
	v_add_f32_e32 v38, v100, v38
	v_add_f32_e32 v39, v100, v39
	v_add_f32_e32 v40, v100, v40
	v_mul_f32_e32 v37, v37, v38
	v_mul_f32_e32 v38, v42, v39
	v_mul_f32_e32 v39, v43, v40
	v_mov_b32_e32 v40, v21
	v_cvt_pk_fp8_f32 v40, v37, v38
	v_mul_f32_e32 v37, 0x41000000, v44
	v_add_f32_e32 v38, v100, v41
	v_mul_f32_e32 v37, v37, v38
	v_cvt_pk_fp8_f32 v40, v39, v37 op_sel:[0,0,1]
	global_store_dword v[136:137], v40, off offset:176
	ds_read_b64_tr_b16 v[38:39], v34 offset:384
	ds_read_b64_tr_b16 v[40:41], v34 offset:9088
	ds_read_b64_tr_b16 v[42:43], v34 offset:17792
	ds_read_b64_tr_b16 v[44:45], v34 offset:26496
	ds_read_b64_tr_b16 v[46:47], v34 offset:35200
	ds_read_b64_tr_b16 v[48:49], v34 offset:43904
	ds_read_b64_tr_b16 v[50:51], v34 offset:52608
	ds_read_b64_tr_b16 v[52:53], v34 offset:61312
	s_waitcnt lgkmcnt(0)
; __device__ __forceinline__ void gating_phase(Frame& F) {
;     ...
;         GT_DT(0); GT_DT(1); GT_DT(2); GT_DT(3); GT_DT(4); GT_DT(5); GT_DT(6); GT_DT(7); GT_DT(8); GT_DT(9); GT_DT(10); GT_DT(11); GT_DT(12); GT_DT(13); GT_DT(14); GT_DT(15);
;     ...
;         __syncthreads();
;     }
; }
	v_mfma_f32_16x16x32_bf16 v[38:41], v[38:41], v[84:87], 0
	s_waitcnt vmcnt(15)
	v_lshlrev_b32_e32 v37, 16, v128
	v_mul_f32_e32 v37, 0x41000000, v37
	v_mfma_f32_16x16x32_bf16 v[38:41], v[42:45], v[88:91], v[38:41]
	v_and_b32_e32 v42, 0xffff0000, v128
	v_lshlrev_b32_e32 v43, 16, v129
	v_mul_f32_e32 v42, 0x41000000, v42
	v_mfma_f32_16x16x32_bf16 v[38:41], v[46:49], v[92:95], v[38:41]
	v_mul_f32_e32 v43, 0x41000000, v43
	v_and_b32_e32 v44, 0xffff0000, v129
	v_mfma_f32_16x16x32_bf16 v[38:41], v[50:53], v[96:99], v[38:41]
	s_nop 7
	v_add_f32_e32 v38, v100, v38
	v_add_f32_e32 v39, v100, v39
	v_add_f32_e32 v40, v100, v40
	v_mul_f32_e32 v37, v37, v38
	v_mul_f32_e32 v38, v42, v39
	v_mul_f32_e32 v39, v43, v40
	v_mov_b32_e32 v40, v21
	v_cvt_pk_fp8_f32 v40, v37, v38
	v_mul_f32_e32 v37, 0x41000000, v44
	v_add_f32_e32 v38, v100, v41
	v_mul_f32_e32 v37, v37, v38
	v_cvt_pk_fp8_f32 v40, v39, v37 op_sel:[0,0,1]
	global_store_dword v[136:137], v40, off offset:192
	ds_read_b64_tr_b16 v[38:39], v34 offset:416
	ds_read_b64_tr_b16 v[40:41], v34 offset:9120
	ds_read_b64_tr_b16 v[42:43], v34 offset:17824
	ds_read_b64_tr_b16 v[44:45], v34 offset:26528
	ds_read_b64_tr_b16 v[46:47], v34 offset:35232
	ds_read_b64_tr_b16 v[48:49], v34 offset:43936
	ds_read_b64_tr_b16 v[50:51], v34 offset:52640
	ds_read_b64_tr_b16 v[52:53], v34 offset:61344
	s_waitcnt lgkmcnt(0)
	v_mfma_f32_16x16x32_bf16 v[38:41], v[38:41], v[84:87], 0
	s_waitcnt vmcnt(15)
	v_lshlrev_b32_e32 v37, 16, v130
	v_mul_f32_e32 v37, 0x41000000, v37
	v_mfma_f32_16x16x32_bf16 v[38:41], v[42:45], v[88:91], v[38:41]
	v_and_b32_e32 v42, 0xffff0000, v130
	v_lshlrev_b32_e32 v43, 16, v131
	v_mul_f32_e32 v42, 0x41000000, v42
	v_mfma_f32_16x16x32_bf16 v[38:41], v[46:49], v[92:95], v[38:41]
	v_mul_f32_e32 v43, 0x41000000, v43
	v_and_b32_e32 v44, 0xffff0000, v131
	v_mfma_f32_16x16x32_bf16 v[38:41], v[50:53], v[96:99], v[38:41]
	s_nop 7
	v_add_f32_e32 v38, v100, v38
	v_add_f32_e32 v39, v100, v39
	v_add_f32_e32 v40, v100, v40
	v_mul_f32_e32 v37, v37, v38
	v_mul_f32_e32 v38, v42, v39
	v_mul_f32_e32 v39, v43, v40
	v_mov_b32_e32 v40, v21
	v_cvt_pk_fp8_f32 v40, v37, v38
	v_mul_f32_e32 v37, 0x41000000, v44
	v_add_f32_e32 v38, v100, v41
	v_mul_f32_e32 v37, v37, v38
	v_cvt_pk_fp8_f32 v40, v39, v37 op_sel:[0,0,1]
	global_store_dword v[136:137], v40, off offset:208
	ds_read_b64_tr_b16 v[38:39], v34 offset:448
	ds_read_b64_tr_b16 v[40:41], v34 offset:9152
	ds_read_b64_tr_b16 v[42:43], v34 offset:17856
	ds_read_b64_tr_b16 v[44:45], v34 offset:26560
	ds_read_b64_tr_b16 v[46:47], v34 offset:35264
	ds_read_b64_tr_b16 v[48:49], v34 offset:43968
	ds_read_b64_tr_b16 v[50:51], v34 offset:52672
	ds_read_b64_tr_b16 v[52:53], v34 offset:61376
	s_waitcnt lgkmcnt(0)
	v_mfma_f32_16x16x32_bf16 v[38:41], v[38:41], v[84:87], 0
	s_waitcnt vmcnt(15)
	v_lshlrev_b32_e32 v37, 16, v132
	v_mul_f32_e32 v37, 0x41000000, v37
	v_mfma_f32_16x16x32_bf16 v[38:41], v[42:45], v[88:91], v[38:41]
	v_and_b32_e32 v42, 0xffff0000, v132
	v_lshlrev_b32_e32 v43, 16, v133
	v_mul_f32_e32 v42, 0x41000000, v42
	v_mfma_f32_16x16x32_bf16 v[38:41], v[46:49], v[92:95], v[38:41]
	v_mul_f32_e32 v43, 0x41000000, v43
	v_and_b32_e32 v44, 0xffff0000, v133
	v_mfma_f32_16x16x32_bf16 v[38:41], v[50:53], v[96:99], v[38:41]
	s_nop 7
	v_add_f32_e32 v38, v100, v38
	v_add_f32_e32 v39, v100, v39
	v_add_f32_e32 v40, v100, v40
	v_mul_f32_e32 v37, v37, v38
	v_mul_f32_e32 v38, v42, v39
	v_mul_f32_e32 v39, v43, v40
	v_mov_b32_e32 v40, v21
	v_cvt_pk_fp8_f32 v40, v37, v38
	v_mul_f32_e32 v37, 0x41000000, v44
	v_add_f32_e32 v38, v100, v41
	v_mul_f32_e32 v37, v37, v38
	v_cvt_pk_fp8_f32 v40, v39, v37 op_sel:[0,0,1]
	global_store_dword v[136:137], v40, off offset:224
	ds_read_b64_tr_b16 v[38:39], v34 offset:480
	ds_read_b64_tr_b16 v[40:41], v34 offset:9184
	ds_read_b64_tr_b16 v[42:43], v34 offset:17888
	ds_read_b64_tr_b16 v[44:45], v34 offset:26592
	ds_read_b64_tr_b16 v[46:47], v34 offset:35296
	ds_read_b64_tr_b16 v[48:49], v34 offset:44000
	ds_read_b64_tr_b16 v[50:51], v34 offset:52704
	ds_read_b64_tr_b16 v[52:53], v34 offset:61408
	s_waitcnt lgkmcnt(0)
	v_mfma_f32_16x16x32_bf16 v[38:41], v[38:41], v[84:87], 0
	s_waitcnt vmcnt(15)
	v_lshlrev_b32_e32 v37, 16, v134
	v_mul_f32_e32 v37, 0x41000000, v37
	v_mfma_f32_16x16x32_bf16 v[38:41], v[42:45], v[88:91], v[38:41]
	v_and_b32_e32 v42, 0xffff0000, v134
	v_lshlrev_b32_e32 v43, 16, v135
	v_mul_f32_e32 v42, 0x41000000, v42
	v_mfma_f32_16x16x32_bf16 v[38:41], v[46:49], v[92:95], v[38:41]
	v_mul_f32_e32 v43, 0x41000000, v43
	v_and_b32_e32 v44, 0xffff0000, v135
	v_mfma_f32_16x16x32_bf16 v[38:41], v[50:53], v[96:99], v[38:41]
	s_nop 7
	v_add_f32_e32 v38, v100, v38
	v_add_f32_e32 v39, v100, v39
	v_add_f32_e32 v40, v100, v40
	v_mul_f32_e32 v37, v37, v38
	v_mul_f32_e32 v38, v42, v39
	v_mul_f32_e32 v39, v43, v40
	v_mov_b32_e32 v40, v21
	v_cvt_pk_fp8_f32 v40, v37, v38
	v_mul_f32_e32 v37, 0x41000000, v44
	v_add_f32_e32 v38, v100, v41
	v_mul_f32_e32 v37, v37, v38
	v_cvt_pk_fp8_f32 v40, v39, v37 op_sel:[0,0,1]
	global_store_dword v[136:137], v40, off offset:240
	s_add_i32 s19, s19, s33
	s_cmpk_gt_i32 s19, 0x7ff
	s_barrier
	s_cbranch_scc0 .LBB0_323
